# MoE up/down GEMM units dealt by the XCD-aware virtual workgroup index: the 8 column tiles of a row block share one XCD L2
# speedup vs baseline: 1.0119x; 1.0119x over previous
; #define LAS __attribute__((address_space(3)))
; #define SEAM(k) do { if (IN(k) && IN((k) + 1)) GRID_BAR(); } while (0)
; template <unsigned PHMASK> __global__ void __launch_bounds__(NTHR, 2) fwd(Args args) {
;     extern __shared__ __attribute__((aligned(16))) unsigned char lds_raw[];
;     Frame F;
;     F.lds = (LAS unsigned char*)lds_raw; F.ws = args.ws; F.ctl = (gu32*)(args.ws + WS_CTL);
;     F.tid = threadIdx.x; F.lane = F.tid & 63; F.wave = __builtin_amdgcn_readfirstlane(F.tid >> 6); F.G = gridDim.x; F.bx = blockIdx.x;
;     const int wave0 = F.wave;
;     volatile LAS unsigned* MISC = (volatile LAS unsigned*)(F.lds + MISC_OFF);
;     if (F.tid < 64) MISC[F.tid] = 0u;
;     if (F.tid == 0) { LAS unsigned long long* P = (LAS unsigned long long*)(F.lds + PTR_OFF);
; #pragma unroll
;         for (int i = 0; i < 26; ++i) P[i] = (unsigned long long)args.in[i];
;         P[26] = (unsigned long long)args.out; P[27] = (unsigned long long)args.ws; }
;     __syncthreads();
;     ...
;     XcdBarrier bar = xcd_barrier_post((unsigned*)(F.ctl + CW_BAR), MISC + 8);
;     ...
;     const int lo = args.ph_lo, hi = args.ph_hi;
;     ...
;     if (PHON(0) && IN(0)) for (int dup_ = 0; dup_ < (DUP_PHASE == 0 ? 2 : 1); ++dup_) { PHASE_FENCE(); p0_prologue(args, F); __syncthreads(); } SEAM(0);
;     for (int l = 0; l < DEPTH; ++l) {
;         const int pb = 1 + l * PH_PER_LAYER;
.LBB0_202:
	s_cmpk_lt_i32 s92, 0xdc0
	s_cselect_b64 s[16:17], -1, 0
	s_ashr_i32 s93, s92, 31
	s_lshr_b32 s0, s93, 29
	s_add_i32 s0, s92, s0
	s_ashr_i32 s7, s0, 3
	s_ashr_i32 s53, s52, 31
	s_add_u32 s4, s2, 0x4200
	s_addc_u32 s5, s3, 0
	v_writelane_b32 v249, s4, 7
	s_mov_b32 s18, 2.0
	s_mov_b32 s74, 0x41000000
	v_writelane_b32 v249, s5, 8
	s_add_u32 s4, s2, 0x4400
	s_addc_u32 s5, s3, 0
	v_writelane_b32 v249, s4, 9
	s_mov_b32 s36, 0x41200000
	s_mov_b32 s26, 0x41800000
	v_writelane_b32 v249, s5, 10
	s_add_u32 s4, s2, 0x4500
	s_addc_u32 s5, s3, 0
	v_writelane_b32 v249, s4, 11
	s_mov_b32 s56, 0x41900000
	s_mov_b32 s22, 0x41c00000
	v_writelane_b32 v249, s5, 12
	s_add_u32 s4, s2, 0x4600
	s_addc_u32 s5, s3, 0
	v_writelane_b32 v249, s4, 13
	s_mov_b32 s24, 0x41d00000
	s_mov_b32 s30, 0x42680000
	v_writelane_b32 v249, s5, 14
	s_add_u32 s4, s2, 0x4700
	s_addc_u32 s5, s3, 0
	v_writelane_b32 v249, s4, 15
	s_mov_b32 s20, 0x42600000
	s_mov_b32 s34, 0x42480000
	v_writelane_b32 v249, s5, 16
	s_add_u32 s4, s2, 0x4800
	s_addc_u32 s5, s3, 0
	v_writelane_b32 v249, s4, 17
	s_mov_b32 s80, 0x42400000
	s_mov_b32 s76, 0x42280000
	v_writelane_b32 v249, s5, 18
	s_add_u32 s4, s2, 0x4900
	s_addc_u32 s5, s3, 0
	v_writelane_b32 v249, s4, 19
	s_mov_b32 s82, 0x42200000
	s_mov_b32 s84, 0x42080000
	v_writelane_b32 v249, s5, 20
	s_add_u32 s4, s2, 0x4a00
	s_addc_u32 s5, s3, 0
	v_writelane_b32 v249, s4, 21
	s_mov_b32 s86, 0x42000000
	s_mov_b32 s89, 0
	v_writelane_b32 v249, s5, 22
	s_add_u32 s4, s2, 0x4b00
	s_addc_u32 s5, s3, 0
	v_writelane_b32 v249, s4, 23
	v_mov_b32_e32 v1, 0
	v_mov_b32_e32 v223, 1
	v_writelane_b32 v249, s5, 24
	s_add_u32 s4, s2, 0x4c00
	s_addc_u32 s5, s3, 0
	v_writelane_b32 v249, s4, 25
	v_mov_b32_e32 v224, 1.0
	v_mov_b32_e32 v225, 0x3ecc95a3
	v_writelane_b32 v249, s5, 26
	s_add_u32 s4, s2, 0x4d00
	s_addc_u32 s5, s3, 0
	v_writelane_b32 v249, s4, 27
	v_mov_b32_e32 v226, 0x3c088889
	v_mov_b32_e32 v227, 0x260
	v_writelane_b32 v249, s5, 28
	s_add_u32 s4, s2, 0x4e00
	s_addc_u32 s5, s3, 0
	v_writelane_b32 v249, s4, 29
	s_mov_b32 s19, 0x40400000
	s_mov_b32 s75, 0x41100000
	v_writelane_b32 v249, s5, 30
	s_add_u32 s4, s2, 0x4f00
	s_addc_u32 s5, s3, 0
	v_writelane_b32 v249, s4, 31
	s_mov_b32 s37, 0x41300000
	s_mov_b32 s27, 0x41880000
	v_writelane_b32 v249, s5, 32
	s_add_u32 s4, s2, 0x5000
	s_addc_u32 s5, s3, 0
	v_writelane_b32 v249, s4, 33
	s_mov_b32 s57, 0x41980000
	s_mov_b32 s23, 0x41c80000
	v_writelane_b32 v249, s5, 34
	s_add_u32 s4, s2, 0x5100
	s_addc_u32 s5, s3, 0
	v_writelane_b32 v249, s4, 35
	s_mov_b32 s25, 0x41d80000
	s_mov_b32 s31, 0x426c0000
	v_writelane_b32 v249, s5, 36
	s_add_u32 s4, s2, 0x5200
	s_addc_u32 s5, s3, 0
	v_writelane_b32 v249, s4, 37
	s_mov_b32 s21, 0x42640000
	s_mov_b32 s35, 0x424c0000
	v_writelane_b32 v249, s5, 38
	s_add_u32 s4, s2, 0x5300
	s_addc_u32 s5, s3, 0
	v_writelane_b32 v249, s4, 39
	s_cmp_eq_u32 s33, 15
	s_mov_b32 s81, 0x42440000
	v_writelane_b32 v249, s5, 40
	s_cselect_b64 s[4:5], -1, 0
	v_writelane_b32 v249, s4, 41
	s_cmp_eq_u32 s33, 14
	s_mov_b32 s77, 0x422c0000
	v_writelane_b32 v249, s5, 42
	s_cselect_b64 s[4:5], -1, 0
	v_writelane_b32 v249, s4, 43
	s_cmp_eq_u32 s33, 13
	s_mov_b32 s83, 0x42240000
	v_writelane_b32 v249, s5, 44
	s_cselect_b64 s[4:5], -1, 0
	v_writelane_b32 v249, s4, 45
	s_cmp_eq_u32 s33, 12
	s_mov_b32 s85, 0x420c0000
	v_writelane_b32 v249, s5, 46
	s_cselect_b64 s[4:5], -1, 0
	v_writelane_b32 v249, s4, 47
	s_cmp_eq_u32 s33, 11
	s_mov_b32 s87, 0x42040000
	v_writelane_b32 v249, s5, 48
	s_cselect_b64 s[4:5], -1, 0
	v_writelane_b32 v249, s4, 49
	s_cmp_eq_u32 s33, 10
	v_mov_b32_e32 v229, -1
	v_writelane_b32 v249, s5, 50
	s_cselect_b64 s[4:5], -1, 0
	v_writelane_b32 v249, s4, 51
	s_cmp_eq_u32 s33, 9
	v_mov_b32_e32 v230, 0x3727c5ac
	v_writelane_b32 v249, s5, 52
	s_cselect_b64 s[4:5], -1, 0
	v_writelane_b32 v249, s4, 53
	s_cmp_eq_u32 s33, 8
	v_mov_b64_e32 v[194:195], 0xdbf
	v_writelane_b32 v249, s5, 54
	s_cselect_b64 s[4:5], -1, 0
	v_writelane_b32 v249, s4, 55
	s_cmp_eq_u32 s33, 7
	v_mov_b32_e32 v196, 0x3f317218
	v_writelane_b32 v249, s5, 56
	s_cselect_b64 s[4:5], -1, 0
	v_writelane_b32 v249, s4, 57
	s_cmp_eq_u32 s33, 6
	v_mov_b32_e32 v231, 0x7f800000
	v_writelane_b32 v249, s5, 58
	s_cselect_b64 s[4:5], -1, 0
	v_writelane_b32 v249, s4, 59
	s_cmp_eq_u32 s33, 5
	v_mov_b32_e32 v232, 0x7fc00000
	v_writelane_b32 v249, s5, 60
	s_cselect_b64 s[4:5], -1, 0
	v_writelane_b32 v249, s4, 61
	s_cmp_eq_u32 s33, 4
	v_mov_b32_e32 v233, 0xff800000
	v_writelane_b32 v249, s5, 62
	s_cselect_b64 s[4:5], -1, 0
	v_writelane_b32 v249, s4, 63
	s_cmp_eq_u32 s33, 3
	v_mov_b32_e32 v234, 0x42800000
	v_writelane_b32 v248, s5, 0
	s_cselect_b64 s[4:5], -1, 0
	v_writelane_b32 v248, s4, 1
	s_cmp_eq_u32 s33, 2
	v_mov_b64_e32 v[198:199], 0x1ff
	v_writelane_b32 v248, s5, 2
	s_cselect_b64 s[4:5], -1, 0
	v_writelane_b32 v248, s4, 3
	s_cmp_eq_u32 s33, 1
	s_mov_b32 s94, 0xbe800000
	v_writelane_b32 v248, s5, 4
	s_cselect_b64 s[4:5], -1, 0
	v_writelane_b32 v248, s4, 5
	s_cmp_eq_u32 s33, 0
	s_movk_i32 s95, 0x7fff
	v_writelane_b32 v248, s5, 6
	s_cselect_b64 s[4:5], -1, 0
	s_lshl_b32 s1, s33, 8
	v_writelane_b32 v248, s4, 7
	s_add_u32 s1, s14, s1
	s_movk_i32 s33, 0x6e00
	v_writelane_b32 v248, s5, 8
	s_addc_u32 s4, s15, 0
	s_add_u32 s8, s1, 0x1400
	s_addc_u32 s9, s4, 0
	v_writelane_b32 v248, s8, 9
	s_mov_b64 s[90:91], 0x80
	s_mov_b32 s96, 0xc1000000
	v_writelane_b32 v248, s9, 10
	s_add_u32 s8, s1, 0x2400
	s_addc_u32 s9, s4, 0
	v_writelane_b32 v248, s8, 11
	s_add_u32 s4, s2, 0x7400
	s_addc_u32 s5, s3, 0
	v_writelane_b32 v248, s9, 12
	v_writelane_b32 v248, s4, 13
	s_add_u32 s2, s2, 0x7500
	s_addc_u32 s3, s3, 0
	v_writelane_b32 v248, s5, 14
	v_writelane_b32 v248, s2, 15
; #define GAS __attribute__((address_space(1)))
; __device__ __forceinline__ void nsa_mfma_phase(Frame& F, int l, bf16* YC, int ypitch) {
;     ...
;     const int vcu = (F.G % 8 == 0) ? (F.bx % 8) * (F.G / 8) + F.bx / 8 : F.bx;
; template <unsigned PHMASK> __global__ void __launch_bounds__(NTHR, 2) fwd(Args args) {
;     ...
;             { int rv_[8]; bool ok_[8];
;               int tg = F.tid; asm volatile("" : "+v"(tg)); const int tc = tg < 256 ? tg : 0;
; #pragma unroll
;               for (int i = 0; i < 8; ++i) { pg8::Unit u; ok_[i] = S.next(i, u); const int e_ = ok_[i] ? u.e : 0; const int pos = (ok_[i] ? u.rb : 0) * 256 + tc; const bool in_ = ok_[i] && pos < mcnt[e_];
;                   rv_[i] = *(const GAS int*)(ldst + (size_t)e_ * T + (in_ ? pos : 0)); if (!in_) rv_[i] = 0; }
	s_nop 1
	v_writelane_b32 v248, s3, 16
	s_lshl_b64 s[2:3], s[92:93], 9
	v_writelane_b32 v248, s2, 17
	s_nop 1
	v_writelane_b32 v248, s3, 18
	s_lshl_b64 s[2:3], s[52:53], 9
	v_writelane_b32 v248, s2, 19
	s_cmpk_lt_i32 s92, 0x100
	s_nop 0
	v_writelane_b32 v248, s3, 20
	s_cselect_b64 s[2:3], -1, 0
	s_and_b32 s0, s0, -8
	s_ashr_i32 s1, s52, 3
	s_sub_i32 s8, s92, s0
	v_writelane_b32 v248, s2, 21
	s_mul_i32 s0, s1, s8
	s_add_i32 s1, s0, s7
	v_writelane_b32 v248, s3, 22
	s_lshl_b32 s13, s92, 3
	s_and_b32 s2, s52, 7
	s_lshl_b32 s38, s52, 3
	s_cmpk_lt_i32 s92, 0x200
	s_cselect_b64 s[4:5], -1, 0
	v_writelane_b32 v248, s4, 23
	s_not_b32 s0, s92
	s_ashr_i32 s9, s8, 31
	v_writelane_b32 v248, s5, 24
	s_add_i32 s0, s52, s0
	v_writelane_b32 v248, s0, 25
	s_lshl_b64 s[4:5], s[8:9], 20
	v_writelane_b32 v248, s4, 26
	s_lshl_b32 s3, s8, 6
	s_add_i32 s0, s38, 0x3fff
	v_writelane_b32 v248, s5, 27
	v_readlane_b32 s4, v249, 5
	v_readlane_b32 s5, v249, 6
	s_cmp_gt_i32 s5, 12
	s_cselect_b64 s[4:5], -1, 0
	v_writelane_b32 v248, s4, 28
	s_cmp_lt_i32 s8, 0
	s_mov_b32 s6, s8
	v_writelane_b32 v248, s5, 29
	s_mul_i32 s4, s8, 0x41
	s_cselect_b32 s3, s4, s3
	s_movk_i32 s4, 0x1b9
	s_cselect_b32 s4, s4, 0x1b8
	s_mul_i32 s4, s8, s4
	v_writelane_b32 v248, s6, 30
	s_add_i32 s4, s4, s7
	s_mul_hi_i32 s5, s4, 0x94f2095
	v_writelane_b32 v248, s7, 31
	s_lshr_b32 s6, s5, 31
	s_ashr_i32 s5, s5, 4
	s_add_i32 s5, s5, s6
	s_mul_i32 s6, s5, 0x1b8
	s_lshl_b32 s5, s5, 3
	s_sub_i32 s4, s4, s6
	s_sub_i32 s6, 64, s5
	s_min_i32 s6, s6, 8
	s_cmp_eq_u32 s2, 0
	s_cselect_b32 s1, s1, s92
	s_cmpk_lt_i32 s1, 0x400
	s_cselect_b64 s[8:9], -1, 0
	s_add_i32 s11, s52, s92
	v_writelane_b32 v248, s1, 32
	s_ashr_i32 s10, s11, 31
	v_writelane_b32 v248, s8, 33
	s_lshr_b32 s10, s10, 29
	s_add_i32 s10, s11, s10
	v_writelane_b32 v248, s9, 34
	v_writelane_b32 v248, s7, 35
	s_ashr_i32 s10, s10, 3
	v_writelane_b32 v248, s10, 36
	v_writelane_b32 v248, s11, 37
	s_add_i32 s11, s11, s52
	s_ashr_i32 s10, s11, 31
	s_lshr_b32 s10, s10, 29
	s_add_i32 s10, s11, s10
	s_ashr_i32 s10, s10, 3
	v_writelane_b32 v248, s10, 38
	v_writelane_b32 v248, s11, 39
	s_add_i32 s11, s11, s52
	s_ashr_i32 s10, s11, 31
	s_lshr_b32 s10, s10, 29
	s_add_i32 s10, s11, s10
	s_add_i32 s1, s3, s7
	s_ashr_i32 s10, s10, 3
	s_ashr_i32 s2, s1, 31
	v_writelane_b32 v248, s10, 40
	s_lshr_b32 s2, s2, 26
	v_writelane_b32 v248, s11, 41
	s_add_i32 s11, s11, s52
	s_add_i32 s2, s1, s2
	s_ashr_i32 s10, s11, 31
	s_and_b32 s3, s2, 0xffffffc0
	s_lshr_b32 s10, s10, 29
	s_sub_i32 s1, s1, s3
	s_abs_i32 s3, s6
	s_add_i32 s10, s11, s10
	v_cvt_f32_u32_e32 v0, s3
	s_ashr_i32 s10, s10, 3
	v_writelane_b32 v248, s10, 42
	v_writelane_b32 v248, s11, 43
	s_add_i32 s11, s11, s52
	s_ashr_i32 s10, s11, 31
	v_rcp_iflag_f32_e32 v0, v0
	s_lshr_b32 s10, s10, 29
	s_add_i32 s10, s11, s10
	s_ashr_i32 s10, s10, 3
	v_writelane_b32 v248, s10, 44
	v_mul_f32_e32 v0, 0x4f7ffffe, v0
	v_writelane_b32 v248, s11, 45
	s_add_i32 s11, s11, s52
	v_cvt_u32_f32_e32 v0, v0
	s_ashr_i32 s10, s11, 31
	s_lshr_b32 s10, s10, 29
	s_add_i32 s10, s11, s10
	s_ashr_i32 s10, s10, 3
	s_sub_i32 s7, 0, s3
	v_readfirstlane_b32 s8, v0
	v_writelane_b32 v248, s10, 46
	s_mul_i32 s7, s7, s8
	v_writelane_b32 v248, s11, 47
	s_add_i32 s11, s11, s52
	s_mul_hi_u32 s7, s8, s7
	s_ashr_i32 s10, s11, 31
	s_add_i32 s8, s8, s7
	s_abs_i32 s7, s4
	s_lshr_b32 s10, s10, 29
	s_mul_hi_u32 s8, s7, s8
	s_ashr_i32 s2, s2, 6
	s_add_i32 s10, s11, s10
	s_mul_i32 s9, s8, s3
	s_lshl_b32 s2, s2, 3
	v_writelane_b32 v248, s11, 48
	s_ashr_i32 s10, s10, 3
	s_sub_i32 s7, s7, s9
	s_sub_i32 s9, 64, s2
	v_writelane_b32 v248, s10, 49
	s_xor_b32 s10, s4, s6
	s_min_i32 s9, s9, 8
	s_ashr_i32 s10, s10, 31
	s_add_i32 s11, s8, 1
	s_sub_i32 s12, s7, s3
	s_cmp_ge_u32 s7, s3
	s_cselect_b32 s8, s11, s8
	s_cselect_b32 s7, s12, s7
	s_add_i32 s11, s8, 1
	s_cmp_ge_u32 s7, s3
	s_cselect_b32 s3, s11, s8
	s_xor_b32 s3, s3, s10
	s_sub_i32 s3, s3, s10
	v_writelane_b32 v248, s3, 50
	s_mul_i32 s3, s3, s6
	s_sub_i32 s3, s4, s3
	s_add_i32 s3, s5, s3
	v_writelane_b32 v248, s3, 51
	s_abs_i32 s3, s9
	v_cvt_f32_u32_e32 v0, s3
	s_sub_i32 s4, 0, s3
	v_writelane_b32 v248, s16, 52
	v_rcp_iflag_f32_e32 v0, v0
	s_nop 0
	v_writelane_b32 v248, s17, 53
	v_cndmask_b32_e64 v222, 0, 1, s[16:17]
	s_mov_b32 s17, 0xff800000
	v_mul_f32_e32 v0, 0x4f7ffffe, v0
	v_cvt_u32_f32_e32 v0, v0
	s_nop 0
	v_readfirstlane_b32 s5, v0
	s_mul_i32 s4, s4, s5
	s_mul_hi_u32 s4, s5, s4
	s_add_i32 s5, s5, s4
	s_abs_i32 s4, s1
	s_mul_hi_u32 s5, s4, s5
	s_mul_i32 s6, s5, s3
	s_sub_i32 s4, s4, s6
	s_xor_b32 s6, s1, s9
	s_ashr_i32 s6, s6, 31
	s_add_i32 s7, s5, 1
	s_sub_i32 s8, s4, s3
	s_cmp_ge_u32 s4, s3
	s_cselect_b32 s5, s7, s5
	s_cselect_b32 s4, s8, s4
	s_add_i32 s7, s5, 1
	s_cmp_ge_u32 s4, s3
	s_cselect_b32 s3, s7, s5
	s_xor_b32 s3, s3, s6
	s_sub_i32 s8, s3, s6
	s_mul_i32 s3, s8, s9
	s_sub_i32 s1, s1, s3
	s_abs_i32 s3, s38
	v_cvt_f32_u32_e32 v0, s3
	s_sub_i32 s4, 0, s3
	s_ashr_i32 s9, s8, 31
	s_lshl_b64 s[14:15], s[8:9], 20
	v_rcp_iflag_f32_e32 v0, v0
	s_nop 0
	v_mul_f32_e32 v0, 0x4f7ffffe, v0
	v_cvt_u32_f32_e32 v0, v0
	s_nop 0
	v_readfirstlane_b32 s5, v0
	s_mul_i32 s4, s4, s5
	s_mul_hi_u32 s4, s5, s4
	s_add_i32 s5, s5, s4
	s_abs_i32 s4, s0
	s_mul_hi_u32 s5, s4, s5
	s_mul_i32 s6, s5, s3
	s_sub_i32 s4, s4, s6
	s_add_i32 s6, s2, s1
	s_ashr_i32 s7, s6, 31
	s_xor_b32 s0, s0, s38
	s_ashr_i32 s0, s0, 31
	s_add_i32 s1, s5, 1
	s_sub_i32 s2, s4, s3
	s_lshl_b64 s[10:11], s[6:7], 20
	s_cmp_ge_u32 s4, s3
	s_cselect_b32 s1, s1, s5
	s_cselect_b32 s2, s2, s4
	s_add_i32 s4, s1, 1
	s_cmp_ge_u32 s2, s3
	s_cselect_b32 s1, s4, s1
	s_xor_b32 s1, s1, s0
	s_sub_i32 s2, s1, s0
	s_cmp_gt_i32 s2, 0
	s_cselect_b64 s[0:1], -1, 0
	v_writelane_b32 v248, s0, 54
; #define GAS __attribute__((address_space(1)))
; template <unsigned PHMASK> __global__ void __launch_bounds__(NTHR, 2) fwd(Args args) {
;     ...
;         if ((PHON(9) || PHON(10)) && (IN(pb + 8) || IN(pb + 9))) { const int nu = __builtin_amdgcn_readfirstlane(mblk[16]) * 8; moe_heavy = (nu % F.G != 0) && (F.bx < nu % F.G); moe_q = nu / F.G; moe_h = nu % F.G; }
;         if (PHON(9) && IN(pb + 8)) for (int dup_ = 0; dup_ < (DUP_PHASE == 9 ? 2 : 1); ++dup_) { PHASE_FENCE();
;             pg8::MoeOrder S; S.A = (const char*)(F.ws + WS_X1B); S.B = (const char*)(lw + LW_GU); S.tstepA = 0; S.tstepB = (size_t)256 * DM * 2; S.estepB = (size_t)2048 * DM * 2;
;             S.blk_start = mblk; S.rows = mrows; S.nN = 8; S.G = F.G; S.c = F.bx;
;             { int rv_[8]; bool ok_[8];
;               int tg = F.tid; asm volatile("" : "+v"(tg)); const int tc = tg < 256 ? tg : 0;
; #pragma unroll
;               for (int i = 0; i < 8; ++i) { pg8::Unit u; ok_[i] = S.next(i, u); const int e_ = ok_[i] ? u.e : 0; const int pos = (ok_[i] ? u.rb : 0) * 256 + tc; const bool in_ = ok_[i] && pos < mcnt[e_];
;                   rv_[i] = *(const GAS int*)(ldst + (size_t)e_ * T + (in_ ? pos : 0)); if (!in_) rv_[i] = 0; }
;     ...
;             S.blk_start = mblk; S.rows = nullptr; S.nN = 8; S.G = F.G; S.c = F.G - 1 - F.bx;
;             if (moe_h > 0 && 2 * moe_h <= F.G && moe_q >= 1) { S.nfull = moe_q - 1; S.G2 = F.G - moe_h; S.c2 = F.bx >= moe_h ? F.bx - moe_h : -1; }
	s_ashr_i32 s39, s38, 31
	s_nop 0
	v_writelane_b32 v248, s1, 55
	s_abs_i32 s0, s52
	v_cvt_f32_u32_e32 v0, s0
	v_writelane_b32 v248, s0, 56
	s_sub_i32 s0, 0, s0
	v_rcp_iflag_f32_e32 v0, v0
	s_nop 0
	v_mul_f32_e32 v0, 0x4f7ffffe, v0
	v_cvt_u32_f32_e32 v0, v0
	s_nop 0
	v_readfirstlane_b32 s1, v0
	s_mul_i32 s0, s0, s1
	s_mul_hi_u32 s0, s1, s0
	s_add_i32 s0, s1, s0
	v_writelane_b32 v248, s0, 57
	s_lshl_b32 s0, s6, 8
	v_writelane_b32 v248, s0, 58
	s_lshl_b32 s0, s8, 8
	v_writelane_b32 v248, s0, 59
	s_lshl_b32 s0, s92, 9
	v_writelane_b32 v248, s0, 60
	s_lshl_b32 s0, s52, 9
	v_writelane_b32 v248, s0, 61
	s_lshl_b32 s0, s92, 7
	v_writelane_b32 v248, s0, 62
	s_lshl_b32 s0, s52, 7
	v_writelane_b32 v248, s0, 63
	s_mov_b32 s0, s6
	v_writelane_b32 v247, s0, 0
	v_mbcnt_lo_u32_b32 v0, -1, 0
	s_nop 0
	v_writelane_b32 v247, s1, 1
	s_lshl_b64 s[0:1], s[6:7], 17
	v_writelane_b32 v247, s0, 2
	v_mbcnt_hi_u32_b32 v228, -1, v0
	s_movk_i32 s6, 0x1800
	v_writelane_b32 v247, s1, 3
	s_mov_b32 s0, s8
	v_writelane_b32 v247, s0, 4
	s_nop 1
	v_writelane_b32 v247, s1, 5
	s_lshl_b64 s[0:1], s[8:9], 17
	v_writelane_b32 v247, s0, 6
	s_mov_b32 s8, s89
	s_nop 0
	v_writelane_b32 v247, s1, 7
	s_lshl_b64 s[0:1], s[92:93], 12
	v_writelane_b32 v247, s0, 8
	s_nop 1
	v_writelane_b32 v247, s1, 9
	s_lshl_b64 s[0:1], s[52:53], 12
	v_writelane_b32 v247, s0, 10
	s_nop 1
	v_writelane_b32 v247, s1, 11
	s_lshl_b64 s[0:1], s[38:39], 2
	v_writelane_b32 v247, s0, 12
	s_nop 1
	v_writelane_b32 v247, s1, 13
	s_add_u32 s0, s14, 0x11b00100
	v_writelane_b32 v247, s0, 14
	v_writelane_b32 v247, s14, 15
	s_addc_u32 s0, s15, 0
	s_nop 0
	v_writelane_b32 v247, s15, 16
	v_writelane_b32 v247, s0, 17
	s_add_u32 s0, s10, 0x6a880080
	s_addc_u32 s1, s11, 0
	v_writelane_b32 v247, s0, 18
	s_movk_i32 s15, 0x200
	s_mov_b32 s14, 0x3fb504f3
	v_writelane_b32 v247, s1, 19
	s_add_u32 s0, s10, 0x6a800100
	v_writelane_b32 v247, s10, 20
	s_addc_u32 s1, s11, 0
	s_add_i32 s7, 0, 0x14400
	v_writelane_b32 v247, s11, 21
	v_writelane_b32 v247, s0, 22
	s_nop 1
	v_writelane_b32 v247, s1, 23
	s_ashr_i32 s0, s13, 31
	v_writelane_b32 v247, s0, 24
	v_writelane_b32 v247, s13, 25
	s_add_i32 s0, s38, s13
	v_writelane_b32 v247, s0, 26
	v_writelane_b32 v247, s52, 27
	s_lshl_b32 s0, s52, 4
	s_nop 0
	v_writelane_b32 v247, s53, 28
	v_writelane_b32 v247, s0, 29
	s_add_i32 s0, 0, 0x231d8
	v_writelane_b32 v247, s0, 30
	s_add_i32 s0, 0, 0x23020
	v_writelane_b32 v247, s0, 31
	s_add_i32 s0, 0, 0x23024
	v_writelane_b32 v247, s0, 32
	s_add_i32 s0, 0, 0x23118
	v_writelane_b32 v247, s0, 33
	s_add_i32 s0, 0, 0x23128
	v_writelane_b32 v247, s0, 34
	s_add_i32 s0, 0, 0x23140
	v_writelane_b32 v247, s0, 35
	s_add_i32 s0, 0, 0x23150
	v_writelane_b32 v247, s0, 36
	s_add_i32 s0, 0, 0xc400
	v_writelane_b32 v247, s0, 37
	s_add_i32 s0, 0, 0x1d400
	v_writelane_b32 v247, s0, 38
	s_add_i32 s0, 0, 0x1d800
	v_writelane_b32 v247, s0, 39
	s_add_i32 s0, 0, 0x1e400
	v_writelane_b32 v247, s0, 40
	s_add_i32 s0, 0, 0x1dc00
	v_writelane_b32 v247, s0, 41
	s_add_i32 s0, 0, 0x16980
	v_writelane_b32 v247, s0, 42
	s_add_i32 s0, 0, 0x23190
	v_writelane_b32 v247, s0, 43
	s_add_i32 s0, 0, 0x231a0
	v_writelane_b32 v247, s0, 44
	s_add_i32 s0, 0, 0x20600
	v_writelane_b32 v247, s0, 45
	s_add_i32 s0, 0, 0x20640
	v_writelane_b32 v247, s0, 46
	s_add_i32 s0, 0, 0x20200
	v_writelane_b32 v247, s0, 47
	s_add_i32 s0, 0, 0x20400
	v_writelane_b32 v247, s0, 48
	s_add_i32 s0, 0, 0x20080
	v_writelane_b32 v247, s0, 49
	s_add_i32 s0, 0, 0x20044
	v_writelane_b32 v247, s0, 50
	s_add_i32 s0, 0, 0x2004c
	v_writelane_b32 v247, s0, 51
	s_add_i32 s0, 0, 0x20054
	v_writelane_b32 v247, s0, 52
	s_add_i32 s0, 0, 0x2005c
	v_writelane_b32 v247, s0, 53
	s_add_i32 s0, 0, 0x20064
	v_writelane_b32 v247, s0, 54
	s_add_i32 s0, 0, 0x2006c
	v_writelane_b32 v247, s0, 55
	s_add_i32 s0, 0, 0x20074
	v_writelane_b32 v247, s0, 56
	s_add_i32 s0, 0, 0x2007c
	v_writelane_b32 v247, s0, 57
	s_add_i32 s0, 0, 0x20100
	v_writelane_b32 v247, s0, 58
	s_add_i32 s0, 0, 0x231d0
	v_writelane_b32 v247, s0, 59
	s_lshl_b64 s[0:1], s[38:39], 12
	v_writelane_b32 v247, s0, 60
	s_nop 1
	v_writelane_b32 v247, s1, 61
	s_mov_b32 s0, s38
	v_writelane_b32 v247, s0, 62
	s_nop 1
	v_writelane_b32 v247, s1, 63
	s_lshl_b64 s[0:1], s[38:39], 13
	v_writelane_b32 v246, s0, 0
	s_nop 1
	v_writelane_b32 v246, s1, 1
	s_mov_b64 s[0:1], -1
	v_writelane_b32 v246, s0, 2
	s_nop 1
	v_writelane_b32 v246, s1, 3
	v_writelane_b32 v246, s92, 4
	s_nop 1
	v_writelane_b32 v246, s93, 5
	v_writelane_b32 v246, s2, 6
	v_readlane_b32 s100, v248, 32
	s_not_b32 s101, s100
	s_add_i32 s101, s52, s101
	v_writelane_b32 v248, s101, 25
	s_and_b32 s101, s100, 7
	v_writelane_b32 v248, s101, 30
	s_lshl_b32 s101, s101, 20
	v_writelane_b32 v248, s101, 26
	s_mov_b32 s101, 0
	v_writelane_b32 v248, s101, 27
	s_lshr_b32 s101, s100, 3
	v_writelane_b32 v248, s101, 31
	v_writelane_b32 v248, s101, 35
	s_mov_b32 vcc_lo, s100
	s_add_i32 vcc_lo, vcc_lo, s52
	s_ashr_i32 s101, vcc_lo, 3
	v_writelane_b32 v248, vcc_lo, 37
	v_writelane_b32 v248, s101, 36
	s_add_i32 vcc_lo, vcc_lo, s52
	s_ashr_i32 s101, vcc_lo, 3
	v_writelane_b32 v248, vcc_lo, 39
	v_writelane_b32 v248, s101, 38
	s_add_i32 vcc_lo, vcc_lo, s52
	s_ashr_i32 s101, vcc_lo, 3
	v_writelane_b32 v248, vcc_lo, 41
	v_writelane_b32 v248, s101, 40
	s_add_i32 vcc_lo, vcc_lo, s52
	s_ashr_i32 s101, vcc_lo, 3
	v_writelane_b32 v248, vcc_lo, 43
	v_writelane_b32 v248, s101, 42
	s_add_i32 vcc_lo, vcc_lo, s52
	s_ashr_i32 s101, vcc_lo, 3
	v_writelane_b32 v248, vcc_lo, 45
	v_writelane_b32 v248, s101, 44
	s_add_i32 vcc_lo, vcc_lo, s52
	s_ashr_i32 s101, vcc_lo, 3
	v_writelane_b32 v248, vcc_lo, 47
	v_writelane_b32 v248, s101, 46
	s_add_i32 vcc_lo, vcc_lo, s52
	s_ashr_i32 s101, vcc_lo, 3
	v_writelane_b32 v248, vcc_lo, 48
	v_writelane_b32 v248, s101, 49
	s_branch .LBB0_206

; #define GAS __attribute__((address_space(1)))
;     __device__ __forceinline__ bool next(int i, Unit& u) const {
;         if (i >= nfull && c2 < 0) return false;
;         const int L = i < nfull ? i * G + c : nfull * G + (i - nfull) * G2 + c2; const int nb = __builtin_amdgcn_readfirstlane(blk_start[16]);
;         if (L >= nb * nN) return false;
;         const int rbg = L / nN; u.pn = L - rbg * nN; u.pm = rbg;
;         int e = 0, st = 0;
; #pragma unroll
;         for (int k = 1; k < 16; ++k) { const int bs = __builtin_amdgcn_readfirstlane(blk_start[k]); if (bs <= rbg) { e = k; st = bs; } }
;         u.e = e; u.rb = rbg - st; return true;
; template <unsigned PHMASK> __global__ void __launch_bounds__(NTHR, 2) fwd(Args args) {
;     ...
;         if ((PHON(9) || PHON(10)) && (IN(pb + 8) || IN(pb + 9))) { const int nu = __builtin_amdgcn_readfirstlane(mblk[16]) * 8; moe_heavy = (nu % F.G != 0) && (F.bx < nu % F.G); moe_q = nu / F.G; moe_h = nu % F.G; }
;         if (PHON(9) && IN(pb + 8)) for (int dup_ = 0; dup_ < (DUP_PHASE == 9 ? 2 : 1); ++dup_) { PHASE_FENCE();
;             pg8::MoeOrder S; S.A = (const char*)(F.ws + WS_X1B); S.B = (const char*)(lw + LW_GU); S.tstepA = 0; S.tstepB = (size_t)256 * DM * 2; S.estepB = (size_t)2048 * DM * 2;
;             S.blk_start = mblk; S.rows = mrows; S.nN = 8; S.G = F.G; S.c = F.bx;
;             { int rv_[8]; bool ok_[8];
;               int tg = F.tid; asm volatile("" : "+v"(tg)); const int tc = tg < 256 ? tg : 0;
; #pragma unroll
;               for (int i = 0; i < 8; ++i) { pg8::Unit u; ok_[i] = S.next(i, u); const int e_ = ok_[i] ? u.e : 0; const int pos = (ok_[i] ? u.rb : 0) * 256 + tc; const bool in_ = ok_[i] && pos < mcnt[e_];
;                   rv_[i] = *(const GAS int*)(ldst + (size_t)e_ * T + (in_ ? pos : 0)); if (!in_) rv_[i] = 0; }
.LBB0_1011:
	v_readlane_b32 s0, v247, 49
	v_readlane_b32 s8, v247, 27
	v_readlane_b32 s9, v247, 28
	v_mov_b32_e32 v0, s0
	ds_read_b32 v0, v0
	v_readlane_b32 s3, v248, 57
	s_waitcnt lgkmcnt(0)
	v_readfirstlane_b32 s0, v0
	s_lshl_b32 s1, s0, 3
	s_bfe_i32 s0, s0, 0x1001c
	s_abs_i32 s2, s1
	s_xor_b32 s0, s0, s9
	s_mul_hi_u32 s3, s2, s3
	v_readlane_b32 s9, v248, 56
	s_mul_i32 s4, s3, s9
	s_sub_i32 s2, s2, s4
	s_add_i32 s5, s3, 1
	s_sub_i32 s4, s2, s9
	s_cmp_ge_u32 s2, s9
	s_cselect_b32 s3, s5, s3
	s_cselect_b32 s2, s4, s2
	s_add_i32 s4, s3, 1
	s_cmp_ge_u32 s2, s9
	s_cselect_b32 s2, s4, s3
	s_xor_b32 s2, s2, s0
	s_sub_i32 s0, s2, s0
	v_writelane_b32 v246, s0, 32
	s_mul_i32 s0, s0, s8
	s_sub_i32 s70, s1, s0
	s_cmp_lg_u32 s70, 0
	s_cselect_b64 s[0:1], -1, 0
	v_readlane_b32 s101, v248, 32
	s_cmp_lt_i32 s101, s70
	s_cselect_b64 s[2:3], -1, 0
	s_and_b64 s[58:59], s[0:1], s[2:3]
.LBB0_1012:
	s_xor_b64 s[0:1], s[58:59], -1
	v_writelane_b32 v246, s0, 33
	s_nop 1
	v_writelane_b32 v246, s1, 34
	s_nop 0
	v_readlane_b32 s0, v246, 8
	v_readlane_b32 s1, v246, 9
	s_mov_b32 s1, s89
	v_writelane_b32 v246, s0, 8
	s_nop 1
	v_writelane_b32 v246, s1, 9
	s_lshl_b64 s[0:1], s[0:1], 21
	s_add_u32 s0, s62, s0
	s_addc_u32 s1, s63, s1
	s_add_u32 s0, s0, 0x100000
	s_addc_u32 s1, s1, 0
	v_writelane_b32 v246, s0, 13
	s_andn2_b64 vcc, exec, s[38:39]
	s_nop 0
	v_writelane_b32 v246, s1, 14
	v_writelane_b32 v246, s58, 15
	s_nop 1
	v_writelane_b32 v246, s59, 16
	s_cbranch_vccnz .LBB0_1114
	s_mov_b32 s0, -1
	v_writelane_b32 v246, s38, 17
	v_mbcnt_lo_u32_b32 v0, s0, 0
	v_mbcnt_hi_u32_b32 v0, s0, v0
	v_readlane_b32 s0, v249, 4
	v_writelane_b32 v246, s39, 18
	s_mov_b32 s88, 0
	v_add_u32_e32 v197, s0, v0
	v_readlane_b32 s0, v247, 30
	v_readlane_b32 s38, v246, 35
	s_nop 0
	v_mov_b32_e32 v0, s0
	v_readlane_b32 s0, v247, 49
	s_waitcnt vmcnt(0) lgkmcnt(0)
	ds_read_b64 v[2:3], v0
	v_mov_b32_e32 v0, v197
	v_mov_b32_e32 v4, s0
	ds_read_b32 v4, v4
	s_waitcnt lgkmcnt(1)
	v_readfirstlane_b32 s28, v2
	v_readfirstlane_b32 s29, v3
	s_waitcnt lgkmcnt(0)
	v_readfirstlane_b32 s0, v4
	s_lshl_b32 s2, s0, 3
	v_readlane_b32 s101, v248, 32
	s_cmp_lt_i32 s101, s2
	s_cselect_b64 s[0:1], -1, 0
	s_cmp_ge_i32 s101, s2
	s_cbranch_scc1 .LBB0_1015
	v_readlane_b32 s2, v247, 50
	v_readlane_b32 s5, v248, 35
	s_nop 0
	v_mov_b32_e32 v2, s2
	ds_read2_b32 v[2:3], v2 offset1:1
	s_waitcnt lgkmcnt(0)
	v_readfirstlane_b32 s4, v2
	s_cmp_le_i32 s4, s5
	s_cselect_b64 s[2:3], -1, 0
	v_cndmask_b32_e64 v2, 0, 1, s[2:3]
	s_and_b64 s[2:3], s[2:3], exec
	v_readfirstlane_b32 s3, v3
	s_cselect_b32 s2, s4, 0
	s_cmp_gt_i32 s3, s5
	s_cselect_b32 s2, s2, s3
	v_readlane_b32 s3, v247, 51
	v_readfirstlane_b32 s4, v2
	s_cselect_b32 s4, s4, 2
	v_mov_b32_e32 v2, s3
	ds_read2_b32 v[2:3], v2 offset1:1
	s_waitcnt lgkmcnt(0)
	v_readfirstlane_b32 s3, v2
	s_cmp_gt_i32 s3, s5
	s_cselect_b32 s2, s2, s3
	v_readfirstlane_b32 s3, v3
	s_cselect_b32 s4, s4, 3
	s_cmp_gt_i32 s3, s5
	s_cselect_b32 s2, s2, s3
	v_readlane_b32 s3, v247, 52
	s_cselect_b32 s4, s4, 4
	s_nop 0
	v_mov_b32_e32 v2, s3
	ds_read2_b32 v[2:3], v2 offset1:1
	s_waitcnt lgkmcnt(0)
	v_readfirstlane_b32 s3, v2
	s_cmp_gt_i32 s3, s5
	s_cselect_b32 s2, s2, s3
	v_readfirstlane_b32 s3, v3
	s_cselect_b32 s4, s4, 5
	s_cmp_gt_i32 s3, s5
	s_cselect_b32 s2, s2, s3
	v_readlane_b32 s3, v247, 53
	s_cselect_b32 s4, s4, 6
	s_nop 0
	v_mov_b32_e32 v2, s3
	ds_read2_b32 v[2:3], v2 offset1:1
	s_waitcnt lgkmcnt(0)
	v_readfirstlane_b32 s3, v2
	s_cmp_gt_i32 s3, s5
	s_cselect_b32 s2, s2, s3
	v_readfirstlane_b32 s3, v3
	s_cselect_b32 s4, s4, 7
	s_cmp_gt_i32 s3, s5
	s_cselect_b32 s2, s2, s3
	v_readlane_b32 s3, v247, 54
	s_cselect_b32 s4, s4, 8
	s_nop 0
	v_mov_b32_e32 v2, s3
	ds_read2_b32 v[2:3], v2 offset1:1
	s_waitcnt lgkmcnt(0)
	v_readfirstlane_b32 s3, v2
	s_cmp_gt_i32 s3, s5
	s_cselect_b32 s2, s2, s3
	v_readfirstlane_b32 s3, v3
	s_cselect_b32 s4, s4, 9
	s_cmp_gt_i32 s3, s5
	s_cselect_b32 s2, s2, s3
	v_readlane_b32 s3, v247, 55
	s_cselect_b32 s4, s4, 10
	s_nop 0
	v_mov_b32_e32 v2, s3
	ds_read2_b32 v[2:3], v2 offset1:1
	s_waitcnt lgkmcnt(0)
	v_readfirstlane_b32 s3, v2
	s_cmp_gt_i32 s3, s5
	s_cselect_b32 s2, s2, s3
	v_readfirstlane_b32 s3, v3
	s_cselect_b32 s4, s4, 11
	s_cmp_gt_i32 s3, s5
	s_cselect_b32 s2, s2, s3
	v_readlane_b32 s3, v247, 56
	s_cselect_b32 s4, s4, 12
	s_nop 0
	v_mov_b32_e32 v2, s3
	ds_read2_b32 v[2:3], v2 offset1:1
	s_waitcnt lgkmcnt(0)
	v_readfirstlane_b32 s3, v2
	s_cmp_gt_i32 s3, s5
	s_cselect_b32 s2, s2, s3
	v_readfirstlane_b32 s3, v3
	s_cselect_b32 s4, s4, 13
	s_cmp_gt_i32 s3, s5
	s_cselect_b32 s2, s2, s3
	v_readlane_b32 s3, v247, 57
	s_cselect_b32 s4, s4, 14
	s_nop 0
	v_mov_b32_e32 v2, s3
	ds_read_b32 v2, v2
	s_waitcnt lgkmcnt(0)
	v_readfirstlane_b32 s3, v2
	s_cmp_gt_i32 s3, s5
	s_cselect_b32 s2, s2, s3
	s_cselect_b32 s88, s4, 15
	s_sub_i32 s38, s5, s2

; #define PG8_STAGE_A(bufoff, kptr, h) do { if constexpr (GATHER) { PG8_STAGE(bufoff, kptr, oa[h]); } else { PG8_STAGE(bufoff, (kptr) + (h) * hstep, voffA); } } while (0)
;     __device__ __forceinline__ bool next(int i, Unit& u) const {
;         if (i >= nfull && c2 < 0) return false;
;         const int L = i < nfull ? i * G + c : nfull * G + (i - nfull) * G2 + c2; const int nb = __builtin_amdgcn_readfirstlane(blk_start[16]);
;         if (L >= nb * nN) return false;
;         const int rbg = L / nN; u.pn = L - rbg * nN; u.pm = rbg;
;         int e = 0, st = 0;
; #pragma unroll
;         for (int k = 1; k < 16; ++k) { const int bs = __builtin_amdgcn_readfirstlane(blk_start[k]); if (bs <= rbg) { e = k; st = bs; } }
;         u.e = e; u.rb = rbg - st; return true;
; template <class Epi, class Sched, bool GATHER, bool SEGHOOK = false>
; __device__ __forceinline__ void gemm_phase(LAS unsigned char* lds, const int K, const Sched& S, const Epi& E, int tid_) {
;     ...
;     { int R, C; stage_rc(tid * 16, R, C); Rst0 = R; Cst0 = C; }
; #pragma unroll
;     for (int i = 0; i < 2; ++i) { int R, C; stage_rc(tid * 16 + i * 8192, R, C); const int Rb = Epi::PERM ? ((R & ~31) + perm32(R & 31)) : R;
;         voffA[i] = (unsigned)(R * K + C) * 2u; voffB[i] = (unsigned)(Rb * K + C) * 2u; oa[0][i] = 0u; oa[1][i] = 0u; }
;     ...
;     const unsigned ldsw = (unsigned)wid * 1024u;
;     const int aoff = lds_byte(wr * 64 + fr, fq * 8), boff = lds_byte(wc * 32 + fr, fq * 8);
;     ...
;     Unit cur, nxt; int ui = 0;
;     if (!S.next(0, cur)) return;
;     if constexpr (GATHER) { PG8_GATHER_OFFS(0); }
;     f32x4 acc[2][2][4][2];
; #pragma unroll
;     for (int a = 0; a < 2; ++a)
; #pragma unroll
;         for (int b = 0; b < 2; ++b)
; #pragma unroll
;             for (int m = 0; m < 4; ++m)
; #pragma unroll
;                 for (int n = 0; n < 2; ++n) acc[a][b][m][n] = (f32x4){0.f, 0.f, 0.f, 0.f};
;     bf16x8 At[4][2], B0[2][2], B1[2][2];
;     const char* cA = S.a_base(cur); const char* cB = S.b_base(cur);
;     PG8_STAGE(PG8_SB(0, 0), cB, voffB); PG8_STAGE(PG8_SB(0, 1), cB + hstep, voffB); PG8_STAGE_A(PG8_SA(0, 0), cA, 0); PG8_STAGE_A(PG8_SA(0, 1), cA, 1);
;     if (wr == 1) PG8_BAR;
;     PG8_WAIT_V(2); PG8_BAR;
;     PG8_STAGE(PG8_SB(1, 0), cB + kstep, voffB); PG8_STAGE_A(PG8_SA(1, 0), cA + kstep, 0); PG8_STAGE(PG8_SB(1, 1), cB + hstep + kstep, voffB);
;     PG8_WAIT_V(6); PG8_BAR;
.LBB0_1055:
	s_or_b64 exec, exec, s[0:1]
	v_readlane_b32 s0, v247, 49
	s_waitcnt vmcnt(5)
	v_mov_b32_e32 v6, v197
	s_waitcnt lgkmcnt(0)
	v_mov_b32_e32 v0, s0
	s_barrier
	ds_read_b32 v0, v0
	s_add_u32 s0, s28, 0x6a800000
	s_addc_u32 s1, s29, 0
	v_readlane_b32 s2, v246, 10
	s_add_u32 s72, s28, s2
	s_waitcnt lgkmcnt(0)
	v_readfirstlane_b32 s2, v0
	s_addc_u32 s12, s29, 0
	s_lshl_b32 s2, s2, 3
	v_readlane_b32 s101, v248, 32
	s_cmp_lt_i32 s101, s2
	v_readfirstlane_b32 s2, v6
	s_cbranch_scc0 .LBB0_1083
	s_waitcnt vmcnt(0)
	v_bfe_i32 v3, v6, 27, 1
	v_lshlrev_b32_e32 v0, 4, v6
	v_lshrrev_b32_e32 v3, 22, v3
	v_add_u32_e32 v3, v0, v3
	v_and_b32_e32 v3, 0xfffffc00, v3
	v_sub_u32_e32 v3, v0, v3
	v_ashrrev_i32_e32 v2, 31, v6
	v_lshrrev_b32_e32 v4, 4, v3
	v_lshrrev_b32_e32 v2, 26, v2
	v_bitop3_b32 v3, v4, v3, 32 bitop3:0x6c
	v_add_u32_e32 v2, v6, v2
	v_ashrrev_i32_e32 v5, 31, v3
	v_ashrrev_i32_e32 v2, 6, v2
	v_lshrrev_b32_e32 v5, 26, v5
	v_lshlrev_b32_e32 v4, 5, v2
	v_add_u32_e32 v5, v3, v5
	v_lshlrev_b32_e32 v2, 3, v2
	v_ashrrev_i32_e32 v7, 6, v5
	v_and_b32_e32 v2, -16, v2
	v_add_u32_e32 v0, 0x2000, v0
	v_and_b32_e32 v5, 0xc0, v5
	v_add_u32_e32 v12, v7, v2
	v_ashrrev_i32_e32 v2, 31, v0
	v_sub_u32_e32 v3, v3, v5
	v_lshrrev_b32_e32 v2, 22, v2
	v_ashrrev_i16_sdwa v3, v223, sext(v3) dst_sel:DWORD dst_unused:UNUSED_PAD src0_sel:DWORD src1_sel:BYTE_0
	v_add_u32_e32 v2, v0, v2
	v_bfe_i32 v3, v3, 0, 16
	v_and_b32_e32 v4, 32, v4
	v_ashrrev_i32_e32 v2, 10, v2
	v_add_lshl_u32 v212, v4, v3, 1
	v_mul_i32_i24_e32 v3, 0x400, v2
	v_sub_u32_e32 v0, v0, v3
	v_lshrrev_b32_e32 v3, 4, v0
	v_bitop3_b32 v0, v3, v0, 32 bitop3:0x6c
	v_ashrrev_i32_e32 v3, 31, v0
	v_lshrrev_b32_e32 v3, 26, v3
	v_add_u32_e32 v3, v0, v3
	v_lshlrev_b32_e32 v5, 3, v2
	v_ashrrev_i32_e32 v4, 6, v3
	v_and_b32_e32 v5, -16, v5
	v_and_b32_e32 v3, 0xc0, v3
	v_add_u32_e32 v5, v4, v5
	v_and_b32_e32 v4, 3, v4
	s_mov_b32 s4, 0xfffe0
	v_sub_u32_e32 v0, v0, v3
	v_and_or_b32 v4, v5, s4, v4
	v_lshrrev_b32_e32 v8, 2, v5
	v_lshlrev_b32_e32 v5, 1, v5
	v_lshlrev_b32_e32 v2, 5, v2
	v_ashrrev_i16_sdwa v0, v223, sext(v0) dst_sel:DWORD dst_unused:UNUSED_PAD src0_sel:DWORD src1_sel:BYTE_0
	v_and_b32_e32 v8, 4, v8
	v_and_b32_e32 v5, 24, v5
	v_and_b32_e32 v2, 32, v2
	v_bfe_i32 v0, v0, 0, 16
	v_or3_b32 v4, v4, v8, v5
	v_add_lshl_u32 v0, v2, v0, 1
	v_lshl_add_u32 v200, v4, 12, v0
	v_and_b32_e32 v0, 3, v7
	v_lshrrev_b32_e32 v2, 2, v12
	v_lshlrev_b32_e32 v3, 1, v12
	v_and_or_b32 v0, v12, s4, v0
	v_and_b32_e32 v2, 4, v2
	v_and_b32_e32 v3, 24, v3
	v_or3_b32 v0, v0, v2, v3
	v_readlane_b32 s4, v247, 50
	v_lshl_add_u32 v202, v0, 12, v212
	s_add_u32 s54, s72, 0x5b00000
	v_mov_b32_e32 v0, s4
	ds_read2_b32 v[2:3], v0 offset1:1
	v_readlane_b32 s4, v247, 51
	s_addc_u32 s55, s12, 0
	s_ashr_i32 s8, s2, 6
	v_mov_b32_e32 v0, s4
	v_readlane_b32 s4, v247, 52
	s_ashr_i32 s3, s2, 8
	s_lshl_b32 s64, s8, 10
	v_mov_b32_e32 v7, s4
	v_readlane_b32 s4, v247, 53
	v_readlane_b32 s9, v248, 35
	v_readlane_b32 s10, v248, 26
	v_mov_b32_e32 v10, s4
	ds_read2_b32 v[4:5], v0 offset1:1
	ds_read2_b32 v[8:9], v7 offset1:1
	ds_read2_b32 v[10:11], v10 offset1:1
	s_waitcnt lgkmcnt(3)
	v_readfirstlane_b32 s4, v2
	s_cmp_gt_i32 s4, s9
	v_readfirstlane_b32 s4, v3
	s_cselect_b32 s5, 0, 0x800000
	s_cmp_gt_i32 s4, s9
	s_waitcnt lgkmcnt(2)
	v_readfirstlane_b32 s4, v4
	s_cselect_b32 s5, s5, 0x1000000
	s_cmp_gt_i32 s4, s9
	v_readfirstlane_b32 s4, v5
	s_cselect_b32 s5, s5, 0x1800000
	s_cmp_gt_i32 s4, s9
	s_waitcnt lgkmcnt(1)
	v_readfirstlane_b32 s4, v8
	s_cselect_b32 s5, s5, 0x2000000
	s_cmp_gt_i32 s4, s9
	v_readfirstlane_b32 s4, v9
	s_cselect_b32 s5, s5, 0x2800000
	s_cmp_gt_i32 s4, s9
	s_waitcnt lgkmcnt(0)
	v_readfirstlane_b32 s4, v10
	s_cselect_b32 s5, s5, 0x3000000
	s_cmp_gt_i32 s4, s9
	v_readfirstlane_b32 s4, v11
	s_cselect_b32 s5, s5, 0x3800000
	s_cmp_gt_i32 s4, s9
	v_readlane_b32 s4, v247, 54
	s_cselect_b32 s5, s5, 0x4000000
	v_readlane_b32 s11, v248, 27
	v_mov_b32_e32 v0, s4
	ds_read2_b32 v[2:3], v0 offset1:1
	v_readlane_b32 s4, v247, 55
	v_mov_b32_e32 v203, v1
	v_mov_b32_e32 v201, v1
	v_mov_b32_e32 v0, s4
	v_readlane_b32 s4, v247, 56
	s_mov_b32 s97, s12
	s_nop 0
	v_mov_b32_e32 v7, s4
	v_readlane_b32 s4, v247, 57
	s_nop 1
	v_mov_b32_e32 v10, s4
	ds_read2_b32 v[4:5], v0 offset1:1
	ds_read2_b32 v[8:9], v7 offset1:1
	ds_read_b32 v0, v10
	s_waitcnt lgkmcnt(3)
	v_readfirstlane_b32 s4, v2
	s_cmp_gt_i32 s4, s9
	v_readfirstlane_b32 s4, v3
	s_cselect_b32 s5, s5, 0x4800000
	s_cmp_gt_i32 s4, s9
	s_waitcnt lgkmcnt(2)
	v_readfirstlane_b32 s4, v4
	s_cselect_b32 s5, s5, 0x5000000
	s_cmp_gt_i32 s4, s9
	v_readfirstlane_b32 s4, v5
	s_cselect_b32 s5, s5, 0x5800000
	s_cmp_gt_i32 s4, s9
	s_waitcnt lgkmcnt(1)
	v_readfirstlane_b32 s4, v8
	s_cselect_b32 s5, s5, 0x6000000
	s_cmp_gt_i32 s4, s9
	v_readfirstlane_b32 s4, v9
	s_cselect_b32 s5, s5, 0x6800000
	s_cmp_gt_i32 s4, s9
	s_waitcnt lgkmcnt(0)
	v_readfirstlane_b32 s4, v0
	s_cselect_b32 s5, s5, 0x7000000
	s_cmp_gt_i32 s4, s9
	s_cselect_b32 s4, s5, 0x7800000
	s_add_u32 s4, s54, s4
	s_addc_u32 s5, s55, 0
	v_lshl_add_u32 v2, v12, 2, 0
	s_add_u32 s10, s4, s10
	v_add_u32_e32 v213, 0x20100, v2
	s_addc_u32 s11, s5, s11
	s_add_i32 s65, s64, 0
	ds_read2st64_b32 v[2:3], v213 offset1:1
	ds_read2st64_b32 v[4:5], v213 offset0:2 offset1:3
	s_add_i32 s66, s65, 0x10000
	s_add_i32 s67, s65, 0x12000
	s_mov_b32 m0, s66
	s_add_u32 s4, s10, 0x80000
	global_load_lds_dwordx4 v202, s[10:11]
	s_mov_b32 m0, s67
	s_addc_u32 s5, s11, 0
	s_add_i32 s68, s65, 0x14000
	global_load_lds_dwordx4 v200, s[10:11]
	s_mov_b32 m0, s68
	s_add_i32 s69, s65, 0x16000
	global_load_lds_dwordx4 v202, s[4:5]
	s_mov_b32 m0, s69
	s_waitcnt lgkmcnt(0)
	v_lshl_add_u32 v0, v2, 12, v212
	global_load_lds_dwordx4 v200, s[4:5]
	s_mov_b32 m0, s65
	s_add_i32 s79, s65, 0x2000
	v_lshl_add_u32 v204, v3, 12, v212
	global_load_lds_dwordx4 v0, s[0:1]
	s_mov_b32 m0, s79
	s_add_i32 s88, s65, 0x4000
	v_lshl_add_u32 v208, v4, 12, v212
	global_load_lds_dwordx4 v204, s[0:1]
	s_mov_b32 m0, s88
	s_add_i32 s38, s65, 0x6000
	v_lshl_add_u32 v206, v5, 12, v212
	global_load_lds_dwordx4 v208, s[0:1]
	s_mov_b32 m0, s38
	s_cmp_eq_u32 s3, 1
	global_load_lds_dwordx4 v206, s[0:1]
	v_lshl_add_u64 v[2:3], s[10:11], 0, v[202:203]
	s_cselect_b64 s[4:5], -1, 0
	s_cmp_lg_u32 s3, 1
	v_lshl_add_u64 v[4:5], s[10:11], 0, v[200:201]
	s_cbranch_scc1 .LBB0_1058
	s_barrier

;     __device__ __forceinline__ bool next(int i, Unit& u) const {
;         if (i >= nfull && c2 < 0) return false;
;         const int L = i < nfull ? i * G + c : nfull * G + (i - nfull) * G2 + c2; const int nb = __builtin_amdgcn_readfirstlane(blk_start[16]);
;         if (L >= nb * nN) return false;
;         const int rbg = L / nN; u.pn = L - rbg * nN; u.pm = rbg;
;         int e = 0, st = 0;
; #pragma unroll
;         for (int k = 1; k < 16; ++k) { const int bs = __builtin_amdgcn_readfirstlane(blk_start[k]); if (bs <= rbg) { e = k; st = bs; } }
;         u.e = e; u.rb = rbg - st; return true;
; template <class Epi, class Sched, bool GATHER, bool SEGHOOK = false>
; __device__ __forceinline__ void gemm_phase(LAS unsigned char* lds, const int K, const Sched& S, const Epi& E, int tid_) {
;     ...
;         const bool has_next = S.next(ui + 1, nxt);
;         const char* nA = has_next ? S.a_base(nxt) : cA; const char* nB = has_next ? S.b_base(nxt) : cB;
.LBB0_1061:
	s_mov_b32 s2, s73
	s_add_i32 s73, s73, 1
	s_cmp_gt_u32 s2, 0xffffe
	s_mov_b64 s[2:3], 0
	s_cbranch_scc1 .LBB0_1064
	v_readlane_b32 s2, v247, 49
	s_nop 1
	v_mov_b32_e32 v2, s2
	ds_read_b32 v2, v2
	v_readlane_b32 s2, v247, 27
	s_mul_i32 s9, s73, s2
	v_readlane_b32 s3, v247, 28
	v_readlane_b32 s101, v248, 32
	s_add_i32 s9, s9, s101
	s_waitcnt lgkmcnt(0)
	v_readfirstlane_b32 s2, v2
	s_lshl_b32 s2, s2, 3
	s_cmp_ge_i32 s9, s2
	s_mov_b64 s[2:3], 0
	s_cbranch_scc1 .LBB0_1064
	s_ashr_i32 s2, s9, 31
	s_lshr_b32 s2, s2, 29
	s_add_i32 s2, s9, s2
	s_ashr_i32 s78, s2, 3
	s_and_b32 s2, s2, -8
	s_sub_i32 s50, s9, s2
	v_readlane_b32 s2, v247, 50
	s_nop 1
	v_mov_b32_e32 v2, s2
	ds_read2_b32 v[2:3], v2 offset1:1
	s_waitcnt lgkmcnt(0)
	v_readfirstlane_b32 s2, v2
	s_cmp_le_i32 s2, s78
	s_cselect_b64 s[2:3], -1, 0
	v_cndmask_b32_e64 v2, 0, 1, s[2:3]
	v_readfirstlane_b32 s2, v3
	v_readlane_b32 s3, v247, 51
	s_cmp_gt_i32 s2, s78
	v_readfirstlane_b32 s2, v2
	v_mov_b32_e32 v2, s3
	ds_read2_b32 v[2:3], v2 offset1:1
	s_cselect_b32 s2, s2, 2
	s_waitcnt lgkmcnt(0)
	v_readfirstlane_b32 s3, v2
	s_cmp_gt_i32 s3, s78
	v_readfirstlane_b32 s3, v3
	s_cselect_b32 s2, s2, 3
	s_cmp_gt_i32 s3, s78
	v_readlane_b32 s3, v247, 52
	s_cselect_b32 s2, s2, 4
	s_nop 0
	v_mov_b32_e32 v2, s3
	ds_read2_b32 v[2:3], v2 offset1:1
	s_waitcnt lgkmcnt(0)
	v_readfirstlane_b32 s3, v2
	s_cmp_gt_i32 s3, s78
	v_readfirstlane_b32 s3, v3
	s_cselect_b32 s2, s2, 5
	s_cmp_gt_i32 s3, s78
	v_readlane_b32 s3, v247, 53
	s_cselect_b32 s2, s2, 6
	s_nop 0
	v_mov_b32_e32 v2, s3
	ds_read2_b32 v[2:3], v2 offset1:1
	s_waitcnt lgkmcnt(0)
	v_readfirstlane_b32 s3, v2
	s_cmp_gt_i32 s3, s78
	v_readfirstlane_b32 s3, v3
	s_cselect_b32 s2, s2, 7
	s_cmp_gt_i32 s3, s78
	v_readlane_b32 s3, v247, 54
	s_cselect_b32 s2, s2, 8
	s_nop 0
	v_mov_b32_e32 v2, s3
	ds_read2_b32 v[2:3], v2 offset1:1
	s_waitcnt lgkmcnt(0)
	v_readfirstlane_b32 s3, v2
	s_cmp_gt_i32 s3, s78
	v_readfirstlane_b32 s3, v3
	s_cselect_b32 s2, s2, 9
	s_cmp_gt_i32 s3, s78
	v_readlane_b32 s3, v247, 55
	s_cselect_b32 s2, s2, 10
	s_nop 0
	v_mov_b32_e32 v2, s3
	ds_read2_b32 v[2:3], v2 offset1:1
	s_waitcnt lgkmcnt(0)
	v_readfirstlane_b32 s3, v2
	s_cmp_gt_i32 s3, s78
	v_readfirstlane_b32 s3, v3
	s_cselect_b32 s2, s2, 11
	s_cmp_gt_i32 s3, s78
	v_readlane_b32 s3, v247, 56
	s_cselect_b32 s2, s2, 12
	s_nop 0
	v_mov_b32_e32 v2, s3
	ds_read2_b32 v[2:3], v2 offset1:1
	s_waitcnt lgkmcnt(0)
	v_readfirstlane_b32 s3, v2
	s_cmp_gt_i32 s3, s78
	v_readfirstlane_b32 s3, v3
	s_cselect_b32 s2, s2, 13
	s_cmp_gt_i32 s3, s78
	v_readlane_b32 s3, v247, 57
	s_cselect_b32 s2, s2, 14
	s_nop 0
	v_mov_b32_e32 v2, s3
	ds_read_b32 v2, v2
	s_waitcnt lgkmcnt(0)
	v_readfirstlane_b32 s3, v2
	s_cmp_gt_i32 s3, s78
	s_cselect_b32 s60, s2, 15
	s_mov_b64 s[2:3], -1

;     __device__ __forceinline__ bool next(int i, Unit& u) const {
;         if (i >= nfull && c2 < 0) return false;
;         const int L = i < nfull ? i * G + c : nfull * G + (i - nfull) * G2 + c2; const int nb = __builtin_amdgcn_readfirstlane(blk_start[16]);
;         if (L >= nb * nN) return false;
;         const int rbg = L / nN; u.pn = L - rbg * nN; u.pm = rbg;
;         int e = 0, st = 0;
; #pragma unroll
;         for (int k = 1; k < 16; ++k) { const int bs = __builtin_amdgcn_readfirstlane(blk_start[k]); if (bs <= rbg) { e = k; st = bs; } }
;         u.e = e; u.rb = rbg - st; return true;
; template <unsigned PHMASK> __global__ void __launch_bounds__(NTHR, 2) fwd(Args args) {
;     ...
;         if (PHON(10) && IN(pb + 9)) for (int dup_ = 0; dup_ < (DUP_PHASE == 10 ? 2 : 1); ++dup_) { PHASE_FENCE();
;             pg8::MoeOrder S; S.A = (const char*)(F.ws + WS_H); S.B = (const char*)(lw + LW_DN); S.tstepA = (size_t)256 * DE * 2; S.tstepB = (size_t)256 * DE * 2; S.estepB = (size_t)DM * DE * 2;
;             S.blk_start = mblk; S.rows = nullptr; S.nN = 8; S.G = F.G; S.c = F.G - 1 - F.bx;
;             if (moe_h > 0 && 2 * moe_h <= F.G && moe_q >= 1) { S.nfull = moe_q - 1; S.G2 = F.G - moe_h; S.c2 = F.bx >= moe_h ? F.bx - moe_h : -1; }
;             pg8::EpiMoeDown E{(bf16*)(F.ws + WS_YM), ldst, lgate, mcnt};
;             pg8::gemm_phase<pg8::EpiMoeDown, pg8::MoeOrder, false>(F.lds + RING_OFF, DE, S, E, F.tid);
.LBB0_1168:
	v_readlane_b32 s2, v249, 5
	v_readlane_b32 s3, v249, 6
	s_cmp_le_i32 s2, s8
	s_cselect_b64 s[2:3], -1, 0
	s_and_b64 s[4:5], s[2:3], s[0:1]
	s_andn2_b64 vcc, exec, s[4:5]
	s_cbranch_vccnz .LBB0_1235
	v_writelane_b32 v246, s4, 24
	s_lshl_b32 s0, s70, 1
	v_readlane_b32 s2, v247, 27
	v_writelane_b32 v246, s5, 25
	s_cmp_gt_i32 s0, s2
	v_readlane_b32 s9, v246, 32
	s_mov_b32 s4, -1
	s_cselect_b64 s[0:1], -1, 0
	s_min_i32 s2, s9, s70
	v_readlane_b32 s3, v247, 28
	v_mbcnt_lo_u32_b32 v0, s4, 0
	s_cmp_lt_i32 s2, 1
	v_mbcnt_hi_u32_b32 v0, s4, v0
	v_readlane_b32 s4, v249, 4
	s_cselect_b64 s[2:3], -1, 0
	v_readlane_b32 s101, v248, 32
	s_cmp_lt_i32 s101, s70
	v_add_u32_e32 v141, s4, v0
	v_readlane_b32 s4, v247, 30
	s_waitcnt vmcnt(0)
	v_mov_b32_e32 v10, v141
	v_mov_b32_e32 v0, s4
	s_cselect_b64 s[4:5], -1, 0
	s_sub_i32 s8, s101, s70
	s_add_i32 s9, s9, -1
	s_or_b64 s[12:13], s[2:3], s[0:1]
	s_and_b64 s[0:1], s[12:13], exec
	s_waitcnt lgkmcnt(0)
	ds_read_b64 v[2:3], v0
	s_cselect_b32 s73, 0x100000, s9
	s_or_b64 s[2:3], s[12:13], s[4:5]
	s_and_b64 s[0:1], s[2:3], exec
	s_cselect_b32 s44, -1, s8
	s_cmp_eq_u32 s73, 0
	s_cselect_b64 s[0:1], -1, 0
	v_writelane_b32 v246, s2, 17
	s_waitcnt lgkmcnt(0)
	v_readfirstlane_b32 s28, v2
	v_readfirstlane_b32 s29, v3
	v_writelane_b32 v246, s3, 18
	s_and_b64 s[2:3], s[0:1], s[2:3]
	s_and_b64 vcc, exec, s[2:3]
	v_readfirstlane_b32 s45, v10
	s_cbranch_vccnz .LBB0_1172
	v_readlane_b32 s2, v247, 49
	s_and_b64 s[0:1], s[0:1], exec
	v_readlane_b32 s0, v248, 25
	v_mov_b32_e32 v0, s2
	ds_read_b32 v0, v0
	s_cselect_b32 s0, s44, s0
	s_waitcnt lgkmcnt(0)
	v_readfirstlane_b32 s1, v0
	s_lshl_b32 s1, s1, 3
	s_cmp_ge_i32 s0, s1
	s_cbranch_scc1 .LBB0_1173
	s_ashr_i32 s1, s0, 31
	s_lshr_b32 s1, s1, 29
	s_add_i32 s1, s0, s1
	s_ashr_i32 s10, s1, 3
	s_and_b32 s1, s1, -8
	s_sub_i32 s2, s0, s1
	v_readlane_b32 s0, v247, 50
	s_mov_b64 s[38:39], -1
	s_nop 0
	v_mov_b32_e32 v0, s0
	ds_read2_b32 v[2:3], v0 offset1:1
	s_waitcnt lgkmcnt(0)
	v_readfirstlane_b32 s3, v2
	s_cmp_le_i32 s3, s10
	s_cselect_b64 s[0:1], -1, 0
	v_cndmask_b32_e64 v0, 0, 1, s[0:1]
	s_and_b64 s[0:1], s[0:1], exec
	v_readfirstlane_b32 s1, v3
	s_cselect_b32 s0, s3, 0
	s_cmp_gt_i32 s1, s10
	s_cselect_b32 s0, s0, s1
	v_readlane_b32 s1, v247, 51
	v_readfirstlane_b32 s3, v0
	s_cselect_b32 s3, s3, 2
	v_mov_b32_e32 v0, s1
	ds_read2_b32 v[2:3], v0 offset1:1
	s_waitcnt lgkmcnt(0)
	v_readfirstlane_b32 s1, v2
	s_cmp_gt_i32 s1, s10
	s_cselect_b32 s0, s0, s1
	v_readfirstlane_b32 s1, v3
	s_cselect_b32 s3, s3, 3
	s_cmp_gt_i32 s1, s10
	s_cselect_b32 s0, s0, s1
	v_readlane_b32 s1, v247, 52
	s_cselect_b32 s3, s3, 4
	s_nop 0
	v_mov_b32_e32 v0, s1
	ds_read2_b32 v[2:3], v0 offset1:1
	s_waitcnt lgkmcnt(0)
	v_readfirstlane_b32 s1, v2
	s_cmp_gt_i32 s1, s10
	s_cselect_b32 s0, s0, s1
	v_readfirstlane_b32 s1, v3
	s_cselect_b32 s3, s3, 5
	s_cmp_gt_i32 s1, s10
	s_cselect_b32 s0, s0, s1
	v_readlane_b32 s1, v247, 53
	s_cselect_b32 s3, s3, 6
	s_nop 0
	v_mov_b32_e32 v0, s1
	ds_read2_b32 v[2:3], v0 offset1:1
	s_waitcnt lgkmcnt(0)
	v_readfirstlane_b32 s1, v2
	s_cmp_gt_i32 s1, s10
	s_cselect_b32 s0, s0, s1
	v_readfirstlane_b32 s1, v3
	s_cselect_b32 s3, s3, 7
	s_cmp_gt_i32 s1, s10
	s_cselect_b32 s0, s0, s1
	v_readlane_b32 s1, v247, 54
	s_cselect_b32 s3, s3, 8
	s_nop 0
	v_mov_b32_e32 v0, s1
	ds_read2_b32 v[2:3], v0 offset1:1
	s_waitcnt lgkmcnt(0)
	v_readfirstlane_b32 s1, v2
	s_cmp_gt_i32 s1, s10
	s_cselect_b32 s0, s0, s1
	v_readfirstlane_b32 s1, v3
	s_cselect_b32 s3, s3, 9
	s_cmp_gt_i32 s1, s10
	s_cselect_b32 s0, s0, s1
	v_readlane_b32 s1, v247, 55
	s_cselect_b32 s3, s3, 10
	s_nop 0
	v_mov_b32_e32 v0, s1
	ds_read2_b32 v[2:3], v0 offset1:1
	s_waitcnt lgkmcnt(0)
	v_readfirstlane_b32 s1, v2
	s_cmp_gt_i32 s1, s10
	s_cselect_b32 s0, s0, s1
	v_readfirstlane_b32 s1, v3
	s_cselect_b32 s3, s3, 11
	s_cmp_gt_i32 s1, s10
	s_cselect_b32 s0, s0, s1
	v_readlane_b32 s1, v247, 56
	s_cselect_b32 s3, s3, 12
	s_nop 0
	v_mov_b32_e32 v0, s1
	ds_read2_b32 v[2:3], v0 offset1:1
	s_waitcnt lgkmcnt(0)
	v_readfirstlane_b32 s1, v2
	s_cmp_gt_i32 s1, s10
	s_cselect_b32 s0, s0, s1
	v_readfirstlane_b32 s1, v3
	s_cselect_b32 s3, s3, 13
	s_cmp_gt_i32 s1, s10
	s_cselect_b32 s1, s0, s1
	v_readlane_b32 s0, v247, 57
	s_cselect_b32 s3, s3, 14
	s_nop 0
	v_mov_b32_e32 v0, s0
	ds_read_b32 v0, v0
	s_waitcnt lgkmcnt(0)
	v_readfirstlane_b32 s4, v0
	s_cmp_gt_i32 s4, s10
	s_cselect_b32 s0, s3, 15
	s_cselect_b32 s1, s1, s4
	s_ashr_i32 s11, s10, 31
	s_sub_i32 s46, s10, s1
	s_lshl_b64 s[10:11], s[10:11], 19
	s_branch .LBB0_1174
